# in-place P0 converter also gets the de-serialised LDS read chain
# speedup vs baseline: 1.0057x; 1.0057x over previous
; __device__ __forceinline__ void conv_load(const ConvItem& ci, int lane, float (&v)[64]) {
;     const bool okc = ci.srcc >= 0 && (ci.srcc + lane) < ci.ncols;
;     const float* base = ci.W + (okc ? ci.srcc + lane : 0);
;     const int kmax = ci.Ksrc - 1;
; #pragma unroll
;     for (int i = 0; i < 64; ++i) { const int k = ci.k0 + i, kk = k < kmax ? k : kmax; v[i] = __builtin_nontemporal_load(base + (size_t)kk * ci.ldw); }
; #pragma unroll
;     for (int i = 0; i < 64; ++i) v[i] = (okc && (ci.k0 + i) < ci.Ksrc) ? v[i] : 0.f;
.LBB0_30:
	s_cmp_lt_i32 s58, s76
	s_cselect_b64 s[4:5], -1, 0
	s_and_b64 s[4:5], vcc, s[4:5]
	s_cmp_lt_i32 s64, s76
	s_waitcnt vmcnt(62)
	v_cndmask_b32_e64 v21, 0, v21, s[4:5]
	s_cselect_b64 s[4:5], -1, 0
	s_and_b64 s[4:5], vcc, s[4:5]
	s_cmp_lt_i32 s65, s76
	v_cndmask_b32_e64 v20, 0, v20, s[4:5]
	s_cselect_b64 s[4:5], -1, 0
	s_and_b64 s[4:5], vcc, s[4:5]
	s_cmp_lt_i32 s78, s76
	s_waitcnt vmcnt(61)
	v_cndmask_b32_e64 v19, 0, v19, s[4:5]
	s_cselect_b64 s[4:5], -1, 0
	s_and_b64 s[4:5], vcc, s[4:5]
	s_cmp_lt_i32 s79, s76
	s_waitcnt vmcnt(60)
	v_cndmask_b32_e64 v18, 0, v18, s[4:5]
	s_cselect_b64 s[4:5], -1, 0
	s_and_b64 s[4:5], vcc, s[4:5]
	s_cmp_lt_i32 s80, s76
	s_waitcnt vmcnt(59)
	v_cndmask_b32_e64 v17, 0, v17, s[4:5]
	s_cselect_b64 s[4:5], -1, 0
	s_and_b64 s[4:5], vcc, s[4:5]
	s_cmp_lt_i32 s81, s76
	s_waitcnt vmcnt(58)
	v_cndmask_b32_e64 v16, 0, v16, s[4:5]
	s_cselect_b64 s[4:5], -1, 0
	s_and_b64 s[4:5], vcc, s[4:5]
	s_cmp_lt_i32 s82, s76
	s_waitcnt vmcnt(57)
	v_cndmask_b32_e64 v15, 0, v15, s[4:5]
	s_cselect_b64 s[4:5], -1, 0
	s_and_b64 s[4:5], vcc, s[4:5]
	s_cmp_lt_i32 s83, s76
	s_waitcnt vmcnt(56)
	v_cndmask_b32_e64 v8, 0, v8, s[4:5]
	s_cselect_b64 s[4:5], -1, 0
	s_and_b64 s[4:5], vcc, s[4:5]
	s_cmp_lt_i32 s85, s76
	s_waitcnt vmcnt(55)
	v_cndmask_b32_e64 v29, 0, v29, s[4:5]
	s_cselect_b64 s[4:5], -1, 0
	s_and_b64 s[4:5], vcc, s[4:5]
	s_cmp_lt_i32 s86, s76
	s_waitcnt vmcnt(54)
	v_cndmask_b32_e64 v28, 0, v28, s[4:5]
	s_cselect_b64 s[4:5], -1, 0
	s_and_b64 s[4:5], vcc, s[4:5]
	s_cmp_lt_i32 s87, s76
	s_waitcnt vmcnt(53)
	v_cndmask_b32_e64 v27, 0, v27, s[4:5]
	s_cselect_b64 s[4:5], -1, 0
	s_and_b64 s[4:5], vcc, s[4:5]
	s_cmp_lt_i32 s88, s76
	s_waitcnt vmcnt(52)
	v_cndmask_b32_e64 v26, 0, v26, s[4:5]
	s_cselect_b64 s[4:5], -1, 0
	s_and_b64 s[4:5], vcc, s[4:5]
	s_cmp_lt_i32 s89, s76
	s_waitcnt vmcnt(51)
	v_cndmask_b32_e64 v25, 0, v25, s[4:5]
	s_cselect_b64 s[4:5], -1, 0
	s_and_b64 s[4:5], vcc, s[4:5]
	s_cmp_lt_i32 s90, s76
	s_waitcnt vmcnt(50)
	v_cndmask_b32_e64 v24, 0, v24, s[4:5]
	s_cselect_b64 s[4:5], -1, 0
	s_and_b64 s[4:5], vcc, s[4:5]
	s_cmp_lt_i32 s92, s76
	s_waitcnt vmcnt(49)
	v_cndmask_b32_e64 v23, 0, v23, s[4:5]
	s_cselect_b64 s[4:5], -1, 0
	s_and_b64 s[4:5], vcc, s[4:5]
	s_cmp_lt_i32 s93, s76
	s_waitcnt vmcnt(48)
	v_cndmask_b32_e64 v22, 0, v22, s[4:5]
	s_cselect_b64 s[4:5], -1, 0
	s_and_b64 s[4:5], vcc, s[4:5]
	s_cmp_lt_i32 s94, s76
	s_waitcnt vmcnt(47)
	v_cndmask_b32_e64 v37, 0, v37, s[4:5]
	s_cselect_b64 s[4:5], -1, 0
	s_and_b64 s[4:5], vcc, s[4:5]
	s_cmp_lt_i32 s95, s76
	s_waitcnt vmcnt(46)
	v_cndmask_b32_e64 v36, 0, v36, s[4:5]
	s_cselect_b64 s[4:5], -1, 0
	s_and_b64 s[4:5], vcc, s[4:5]
	s_cmp_lt_i32 s50, s76
	s_waitcnt vmcnt(45)
	v_cndmask_b32_e64 v35, 0, v35, s[4:5]
	s_cselect_b64 s[4:5], -1, 0
	s_and_b64 s[4:5], vcc, s[4:5]
	s_cmp_lt_i32 s51, s76
	s_waitcnt vmcnt(44)
	v_cndmask_b32_e64 v34, 0, v34, s[4:5]
	s_cselect_b64 s[4:5], -1, 0
	s_and_b64 s[4:5], vcc, s[4:5]
	s_cmp_lt_i32 s52, s76
	s_waitcnt vmcnt(43)
	v_cndmask_b32_e64 v33, 0, v33, s[4:5]
	s_cselect_b64 s[4:5], -1, 0
	s_and_b64 s[4:5], vcc, s[4:5]
	s_cmp_lt_i32 s53, s76
	s_waitcnt vmcnt(42)
	v_cndmask_b32_e64 v32, 0, v32, s[4:5]
	s_cselect_b64 s[4:5], -1, 0
	s_and_b64 s[4:5], vcc, s[4:5]
	s_cmp_lt_i32 s6, s76
	s_waitcnt vmcnt(41)
	v_cndmask_b32_e64 v31, 0, v31, s[4:5]
	s_cselect_b64 s[4:5], -1, 0
	s_and_b64 s[4:5], vcc, s[4:5]
	s_cmp_lt_i32 s7, s76
	s_waitcnt vmcnt(40)
	v_cndmask_b32_e64 v30, 0, v30, s[4:5]
	s_cselect_b64 s[4:5], -1, 0
	s_and_b64 s[4:5], vcc, s[4:5]
	s_cmp_lt_i32 s8, s76
	s_waitcnt vmcnt(39)
	v_cndmask_b32_e64 v45, 0, v45, s[4:5]
	s_cselect_b64 s[4:5], -1, 0
	s_and_b64 s[4:5], vcc, s[4:5]
	s_cmp_lt_i32 s9, s76
	s_waitcnt vmcnt(38)
	v_cndmask_b32_e64 v44, 0, v44, s[4:5]
	s_cselect_b64 s[4:5], -1, 0
	s_and_b64 s[4:5], vcc, s[4:5]
	s_cmp_lt_i32 s10, s76
	s_waitcnt vmcnt(37)
	v_cndmask_b32_e64 v43, 0, v43, s[4:5]
	s_cselect_b64 s[4:5], -1, 0
	s_and_b64 s[4:5], vcc, s[4:5]
	s_cmp_lt_i32 s11, s76
	s_waitcnt vmcnt(36)
	v_cndmask_b32_e64 v42, 0, v42, s[4:5]
	s_cselect_b64 s[4:5], -1, 0
	s_and_b64 s[4:5], vcc, s[4:5]
	s_cmp_lt_i32 s14, s76
	s_waitcnt vmcnt(35)
	v_cndmask_b32_e64 v41, 0, v41, s[4:5]
	s_cselect_b64 s[4:5], -1, 0
	s_and_b64 s[4:5], vcc, s[4:5]
	s_cmp_lt_i32 s15, s76
	s_waitcnt vmcnt(34)
	v_cndmask_b32_e64 v40, 0, v40, s[4:5]
	s_cselect_b64 s[4:5], -1, 0
	s_and_b64 s[4:5], vcc, s[4:5]
	s_cmp_lt_i32 s16, s76
	s_waitcnt vmcnt(33)
	v_cndmask_b32_e64 v39, 0, v39, s[4:5]
	s_cselect_b64 s[4:5], -1, 0
	s_and_b64 s[4:5], vcc, s[4:5]
	s_cmp_lt_i32 s17, s76
	s_waitcnt vmcnt(32)
	v_cndmask_b32_e64 v38, 0, v38, s[4:5]
	s_cselect_b64 s[4:5], -1, 0
	s_and_b64 s[4:5], vcc, s[4:5]
	s_cmp_lt_i32 s12, s76
	s_waitcnt vmcnt(31)
	v_cndmask_b32_e64 v53, 0, v53, s[4:5]
	s_cselect_b64 s[4:5], -1, 0
	s_and_b64 s[4:5], vcc, s[4:5]
	s_cmp_lt_i32 s13, s76
	s_waitcnt vmcnt(30)
	v_cndmask_b32_e64 v52, 0, v52, s[4:5]
	s_cselect_b64 s[4:5], -1, 0
	s_and_b64 s[4:5], vcc, s[4:5]
	s_cmp_lt_i32 s20, s76
	s_waitcnt vmcnt(29)
	v_cndmask_b32_e64 v51, 0, v51, s[4:5]
	s_cselect_b64 s[4:5], -1, 0
	s_and_b64 s[4:5], vcc, s[4:5]
	s_cmp_lt_i32 s21, s76
	s_waitcnt vmcnt(28)
	v_cndmask_b32_e64 v50, 0, v50, s[4:5]
	s_cselect_b64 s[4:5], -1, 0
	s_and_b64 s[4:5], vcc, s[4:5]
	s_cmp_lt_i32 s24, s76
	s_waitcnt vmcnt(27)
	v_cndmask_b32_e64 v49, 0, v49, s[4:5]
	s_cselect_b64 s[4:5], -1, 0
	s_and_b64 s[4:5], vcc, s[4:5]
	s_cmp_lt_i32 s25, s76
	s_waitcnt vmcnt(26)
	v_cndmask_b32_e64 v48, 0, v48, s[4:5]
	s_cselect_b64 s[4:5], -1, 0
	s_and_b64 s[4:5], vcc, s[4:5]
	s_cmp_lt_i32 s26, s76
	s_waitcnt vmcnt(25)
	v_cndmask_b32_e64 v47, 0, v47, s[4:5]
	s_cselect_b64 s[4:5], -1, 0
	s_and_b64 s[4:5], vcc, s[4:5]
	s_cmp_lt_i32 s27, s76
	s_waitcnt vmcnt(24)
; #define LAS __attribute__((address_space(3)))
; #define LDS_WAIT() asm volatile("s_waitcnt lgkmcnt(0)" ::: "memory")
; __device__ __forceinline__ void conv_load(const ConvItem& ci, int lane, float (&v)[64]) {
;     ...
;     for (int i = 0; i < 64; ++i) v[i] = (okc && (ci.k0 + i) < ci.Ksrc) ? v[i] : 0.f;
; }
; __device__ __forceinline__ void conv_store(const ConvItem& ci, LAS float* scr, int lane, const float (&v)[64]) {
;     const int c = lane & 7;
;     f32x4 s0 = {1.f, 1.f, 1.f, 1.f}, s1 = s0;
;     if (ci.ks) { const int kb = ci.k0 + 8 * c < ci.Ksrc - 8 ? ci.k0 + 8 * c : ci.Ksrc - 8; s0 = *(const f32x4*)(ci.ks + kb); s1 = *(const f32x4*)(ci.ks + kb + 4); }
; #pragma unroll
;     for (int i = 0; i < 64; ++i) scr[i * 65 + lane] = v[i];
;     LDS_WAIT(); asm volatile("" ::: "memory");
	v_cndmask_b32_e64 v46, 0, v46, s[4:5]
	s_cselect_b64 s[4:5], -1, 0
	s_and_b64 s[4:5], vcc, s[4:5]
	s_cmp_lt_i32 s18, s76
	s_waitcnt vmcnt(23)
	v_cndmask_b32_e64 v61, 0, v61, s[4:5]
	s_cselect_b64 s[4:5], -1, 0
	s_and_b64 s[4:5], vcc, s[4:5]
	s_cmp_lt_i32 s19, s76
	s_waitcnt vmcnt(22)
	v_cndmask_b32_e64 v60, 0, v60, s[4:5]
	s_cselect_b64 s[4:5], -1, 0
	s_and_b64 s[4:5], vcc, s[4:5]
	s_cmp_lt_i32 s28, s76
	s_waitcnt vmcnt(21)
	v_cndmask_b32_e64 v59, 0, v59, s[4:5]
	s_cselect_b64 s[4:5], -1, 0
	s_and_b64 s[4:5], vcc, s[4:5]
	s_cmp_lt_i32 s29, s76
	s_waitcnt vmcnt(20)
	v_cndmask_b32_e64 v58, 0, v58, s[4:5]
	s_cselect_b64 s[4:5], -1, 0
	s_and_b64 s[4:5], vcc, s[4:5]
	s_cmp_lt_i32 s22, s76
	s_waitcnt vmcnt(19)
	v_cndmask_b32_e64 v57, 0, v57, s[4:5]
	s_cselect_b64 s[4:5], -1, 0
	s_and_b64 s[4:5], vcc, s[4:5]
	s_cmp_lt_i32 s23, s76
	s_waitcnt vmcnt(18)
	v_cndmask_b32_e64 v56, 0, v56, s[4:5]
	s_cselect_b64 s[4:5], -1, 0
	s_and_b64 s[4:5], vcc, s[4:5]
	s_cmp_lt_i32 s30, s76
	s_waitcnt vmcnt(17)
	v_cndmask_b32_e64 v55, 0, v55, s[4:5]
	s_cselect_b64 s[4:5], -1, 0
	s_and_b64 s[4:5], vcc, s[4:5]
	s_cmp_lt_i32 s31, s76
	s_waitcnt vmcnt(16)
	v_cndmask_b32_e64 v54, 0, v54, s[4:5]
	s_cselect_b64 s[4:5], -1, 0
	s_and_b64 s[4:5], vcc, s[4:5]
	s_cmp_lt_i32 s36, s76
	s_waitcnt vmcnt(15)
	v_cndmask_b32_e64 v70, 0, v70, s[4:5]
	s_cselect_b64 s[4:5], -1, 0
	s_and_b64 s[4:5], vcc, s[4:5]
	s_cmp_lt_i32 s37, s76
	s_waitcnt vmcnt(14)
	v_cndmask_b32_e64 v69, 0, v69, s[4:5]
	s_cselect_b64 s[4:5], -1, 0
	s_and_b64 s[4:5], vcc, s[4:5]
	s_cmp_lt_i32 s38, s76
	s_waitcnt vmcnt(13)
	v_cndmask_b32_e64 v68, 0, v68, s[4:5]
	s_cselect_b64 s[4:5], -1, 0
	s_and_b64 s[4:5], vcc, s[4:5]
	s_cmp_lt_i32 s39, s76
	s_waitcnt vmcnt(12)
	v_cndmask_b32_e64 v67, 0, v67, s[4:5]
	s_cselect_b64 s[4:5], -1, 0
	s_and_b64 s[4:5], vcc, s[4:5]
	s_cmp_lt_i32 s34, s76
	s_waitcnt vmcnt(11)
	v_cndmask_b32_e64 v66, 0, v66, s[4:5]
	s_cselect_b64 s[4:5], -1, 0
	s_and_b64 s[4:5], vcc, s[4:5]
	s_cmp_lt_i32 s35, s76
	s_waitcnt vmcnt(10)
	v_cndmask_b32_e64 v64, 0, v64, s[4:5]
	s_cselect_b64 s[4:5], -1, 0
	s_and_b64 s[4:5], vcc, s[4:5]
	s_cmp_lt_i32 s42, s76
	s_waitcnt vmcnt(9)
	v_cndmask_b32_e64 v63, 0, v63, s[4:5]
	s_cselect_b64 s[4:5], -1, 0
	s_and_b64 s[4:5], vcc, s[4:5]
	s_cmp_lt_i32 s43, s76
	s_waitcnt vmcnt(8)
	v_cndmask_b32_e64 v62, 0, v62, s[4:5]
	s_cselect_b64 s[4:5], -1, 0
	s_and_b64 s[4:5], vcc, s[4:5]
	s_cmp_lt_i32 s54, s76
	s_waitcnt vmcnt(7)
	v_cndmask_b32_e64 v65, 0, v65, s[4:5]
	s_cselect_b64 s[4:5], -1, 0
	s_and_b64 s[4:5], vcc, s[4:5]
	s_cmp_lt_i32 s55, s76
	s_waitcnt vmcnt(6)
	v_cndmask_b32_e64 v74, 0, v74, s[4:5]
	s_cselect_b64 s[4:5], -1, 0
	s_and_b64 s[4:5], vcc, s[4:5]
	s_cmp_lt_i32 s46, s76
	ds_write2_b32 v12, v21, v20 offset1:65
	ds_write2_b32 v12, v19, v18 offset0:130 offset1:195
	v_add_u32_e32 v18, 0x400, v12
	s_waitcnt vmcnt(5)
	v_cndmask_b32_e64 v73, 0, v73, s[4:5]
	s_cselect_b64 s[4:5], -1, 0
	ds_write2_b32 v18, v17, v16 offset0:4 offset1:69
	ds_write2_b32 v18, v15, v8 offset0:134 offset1:199
	v_add_u32_e32 v8, 0x800, v12
	s_and_b64 s[4:5], vcc, s[4:5]
	ds_write2_b32 v8, v29, v28 offset0:8 offset1:73
	ds_write2_b32 v8, v27, v26 offset0:138 offset1:203
	v_add_u32_e32 v8, 0xc00, v12
	s_cmp_lt_i32 s47, s76
	ds_write2_b32 v8, v25, v24 offset0:12 offset1:77
	ds_write2_b32 v8, v23, v22 offset0:142 offset1:207
	v_add_u32_e32 v8, 0x1000, v12
	s_waitcnt vmcnt(4)
	v_cndmask_b32_e64 v72, 0, v72, s[4:5]
	s_cselect_b64 s[4:5], -1, 0
	ds_write2_b32 v8, v37, v36 offset0:16 offset1:81
	ds_write2_b32 v8, v35, v34 offset0:146 offset1:211
	v_add_u32_e32 v8, 0x1400, v12
	s_and_b64 s[4:5], vcc, s[4:5]
	ds_write2_b32 v8, v33, v32 offset0:20 offset1:85
	ds_write2_b32 v8, v31, v30 offset0:150 offset1:215
	v_add_u32_e32 v8, 0x1800, v12
	s_cmp_lt_i32 s48, s76
	ds_write2_b32 v8, v45, v44 offset0:24 offset1:89
	ds_write2_b32 v8, v43, v42 offset0:154 offset1:219
	v_add_u32_e32 v8, 0x1c00, v12
	s_waitcnt vmcnt(3)
	v_cndmask_b32_e64 v71, 0, v71, s[4:5]
	s_cselect_b64 s[4:5], -1, 0
	ds_write2_b32 v8, v41, v40 offset0:28 offset1:93
	ds_write2_b32 v8, v39, v38 offset0:158 offset1:223
	v_add_u32_e32 v8, 0x2000, v12
	s_and_b64 s[4:5], vcc, s[4:5]
	ds_write2_b32 v8, v53, v52 offset0:32 offset1:97
	ds_write2_b32 v8, v51, v50 offset0:162 offset1:227
	v_add_u32_e32 v8, 0x2400, v12
	s_cmp_lt_i32 s49, s76
	ds_write2_b32 v8, v49, v48 offset0:36 offset1:101
	ds_write2_b32 v8, v47, v46 offset0:166 offset1:231
	v_add_u32_e32 v8, 0x2800, v12
	s_waitcnt vmcnt(2)
	v_cndmask_b32_e64 v77, 0, v77, s[4:5]
	s_cselect_b64 s[4:5], -1, 0
	ds_write2_b32 v8, v61, v60 offset0:40 offset1:105
	ds_write2_b32 v8, v59, v58 offset0:170 offset1:235
	v_add_u32_e32 v8, 0x2c00, v12
	s_and_b64 s[4:5], vcc, s[4:5]
	ds_write2_b32 v8, v57, v56 offset0:44 offset1:109
	ds_write2_b32 v8, v55, v54 offset0:174 offset1:239
	v_add_u32_e32 v8, 0x3000, v12
	s_cmp_lt_i32 s44, s76
	ds_write2_b32 v8, v70, v69 offset0:48 offset1:113
	ds_write2_b32 v8, v68, v67 offset0:178 offset1:243
	v_add_u32_e32 v8, 0x3400, v12
	s_waitcnt vmcnt(1)
	v_cndmask_b32_e64 v76, 0, v76, s[4:5]
	s_cselect_b64 s[4:5], -1, 0
	ds_write2_b32 v8, v66, v64 offset0:52 offset1:117
	ds_write2_b32 v8, v63, v62 offset0:182 offset1:247
	v_add_u32_e32 v8, 0x3800, v12
	s_and_b64 vcc, vcc, s[4:5]
	ds_write2_b32 v8, v65, v74 offset0:56 offset1:121
	ds_write2_b32 v8, v73, v72 offset0:186 offset1:251
	v_add_u32_e32 v8, 0x3c00, v12
	s_waitcnt vmcnt(0)
	v_cndmask_b32_e32 v75, 0, v75, vcc
	ds_write2_b32 v8, v71, v77 offset0:60 offset1:125
	ds_write2_b32 v8, v76, v75 offset0:190 offset1:255
	s_waitcnt lgkmcnt(0)
; __device__ __forceinline__ unsigned cvt_pk_bf16(float lo, float hi) { unsigned r; asm volatile("v_cvt_pk_bf16_f32 %0, %1, %2" : "=v"(r) : "v"(lo), "v"(hi)); return r; }
; #define LAS __attribute__((address_space(3)))
; #define LDS_WAIT() asm volatile("s_waitcnt lgkmcnt(0)" ::: "memory")
; __device__ __forceinline__ void conv_store(const ConvItem& ci, LAS float* scr, int lane, const float (&v)[64]) {
;     ...
;     LDS_WAIT(); asm volatile("" ::: "memory");
; #pragma unroll
;     for (int j = 0; j < 8; ++j) { const int n = (lane >> 3) + 8 * j; const LAS float* s = scr + (8 * c) * 65 + n;
;         v4u o; o.x = cvt_pk_bf16(s[0 * 65] * s0[0], s[1 * 65] * s0[1]); o.y = cvt_pk_bf16(s[2 * 65] * s0[2], s[3 * 65] * s0[3]); o.z = cvt_pk_bf16(s[4 * 65] * s1[0], s[5 * 65] * s1[1]); o.w = cvt_pk_bf16(s[6 * 65] * s1[2], s[7 * 65] * s1[3]);
;         *(v4u*)(ci.dst + (size_t)(ci.drow0 + n) * ci.ldd + ci.k0 + 8 * c) = o; }
	v_add_u32_e32 v192, 0x400, v14
	ds_read2_b32 v[128:129], v14 offset1:65
	ds_read2_b32 v[130:131], v14 offset0:130 offset1:195
	ds_read2_b32 v[132:133], v192 offset0:4 offset1:69
	ds_read2_b32 v[134:135], v192 offset0:134 offset1:199
	ds_read2_b32 v[136:137], v14 offset0:8 offset1:73
	ds_read2_b32 v[138:139], v14 offset0:138 offset1:203
	ds_read2_b32 v[140:141], v192 offset0:12 offset1:77
	ds_read2_b32 v[142:143], v192 offset0:142 offset1:207
	ds_read2_b32 v[144:145], v14 offset0:16 offset1:81
	ds_read2_b32 v[146:147], v14 offset0:146 offset1:211
	ds_read2_b32 v[148:149], v192 offset0:20 offset1:85
	ds_read2_b32 v[150:151], v192 offset0:150 offset1:215
	ds_read2_b32 v[152:153], v14 offset0:24 offset1:89
	ds_read2_b32 v[154:155], v14 offset0:154 offset1:219
	ds_read2_b32 v[156:157], v192 offset0:28 offset1:93
	ds_read2_b32 v[158:159], v192 offset0:158 offset1:223
	ds_read2_b32 v[160:161], v14 offset0:32 offset1:97
	ds_read2_b32 v[162:163], v14 offset0:162 offset1:227
	ds_read2_b32 v[164:165], v192 offset0:36 offset1:101
	ds_read2_b32 v[166:167], v192 offset0:166 offset1:231
	ds_read2_b32 v[168:169], v14 offset0:40 offset1:105
	ds_read2_b32 v[170:171], v14 offset0:170 offset1:235
	ds_read2_b32 v[172:173], v192 offset0:44 offset1:109
	ds_read2_b32 v[174:175], v192 offset0:174 offset1:239
	ds_read2_b32 v[176:177], v14 offset0:48 offset1:113
	ds_read2_b32 v[178:179], v14 offset0:178 offset1:243
	ds_read2_b32 v[180:181], v192 offset0:52 offset1:117
	ds_read2_b32 v[182:183], v192 offset0:182 offset1:247
	ds_read2_b32 v[184:185], v14 offset0:56 offset1:121
	ds_read2_b32 v[186:187], v14 offset0:186 offset1:251
	ds_read2_b32 v[188:189], v192 offset0:60 offset1:125
	ds_read2_b32 v[190:191], v192 offset0:190 offset1:255
	s_waitcnt lgkmcnt(0)
	v_add_u32_e32 v24, s59, v13
	v_mul_lo_u32 v22, s57, v24
	s_ashr_i32 s59, s58, 31
	v_readlane_b32 s76, v254, 31
	s_waitcnt lgkmcnt(0)
	v_mul_f32_e32 v8, v4, v128
	v_mul_f32_e32 v15, v5, v129
	v_cvt_pk_bf16_f32 v16, v8, v15
	s_add_i32 s3, s3, s33
	s_add_i32 s66, s66, s67
	s_add_i32 s68, s68, s69
	s_add_i32 s70, s70, s71
	s_waitcnt lgkmcnt(0)
	v_mul_f32_e32 v15, v7, v131
	v_mul_f32_e32 v8, v6, v130
	v_cvt_pk_bf16_f32 v17, v8, v15
	v_add_u32_e32 v15, 0x400, v14
	s_add_i32 s72, s72, s73
	s_add_i32 s74, s74, s75
	v_readlane_b32 s78, v254, 33
	v_readlane_b32 s79, v254, 34
	s_waitcnt lgkmcnt(0)
	v_mul_f32_e32 v8, v0, v132
	v_mul_f32_e32 v18, v1, v133
	v_cvt_pk_bf16_f32 v18, v8, v18
	v_readlane_b32 s80, v255, 21
	v_readlane_b32 s77, v254, 32
	s_movk_i32 s78, 0x1580
	v_readlane_b32 s82, v255, 23
	s_waitcnt lgkmcnt(0)
	v_mul_f32_e32 v8, v2, v134
	v_mul_f32_e32 v19, v3, v135
	v_cvt_pk_bf16_f32 v19, v8, v19
	v_ashrrev_i32_e32 v8, 31, v24
	v_mul_lo_u32 v8, s56, v8
	v_mad_u64_u32 v[20:21], s[4:5], s56, v24, 0
	v_add3_u32 v21, v21, v8, v22
	v_lshl_add_u64 v[20:21], v[20:21], 1, s[60:61]
	s_lshl_b64 s[4:5], s[58:59], 1
	v_lshl_add_u64 v[20:21], v[20:21], 0, s[4:5]
	v_lshlrev_b32_e32 v8, 1, v10
	v_lshl_add_u64 v[20:21], v[20:21], 0, v[8:9]
	global_store_dwordx4 v[20:21], v[16:19], off
	s_cmp_lt_i32 s3, s99
	v_readlane_b32 s83, v255, 24
	s_waitcnt lgkmcnt(0)
	v_mul_f32_e32 v16, v4, v136
	v_mul_f32_e32 v17, v5, v137
	v_cvt_pk_bf16_f32 v16, v16, v17
	s_mov_b32 s79, 0x3f22f983
	s_mov_b32 s85, 0xbfc90fda
	s_brev_b32 s86, 1
	s_movk_i32 s87, 0x1f8
	s_waitcnt lgkmcnt(0)
	v_mul_f32_e32 v17, v6, v138
	v_mul_f32_e32 v18, v7, v139
	v_cvt_pk_bf16_f32 v17, v17, v18
	s_mov_b64 s[88:89], 0x80
	s_mov_b64 s[92:93], 0x4000
	s_mov_b64 s[94:95], 0x4800
	v_readlane_b32 s81, v255, 22
	s_waitcnt lgkmcnt(0)
	v_mul_f32_e32 v18, v0, v140
	v_mul_f32_e32 v19, v1, v141
	v_cvt_pk_bf16_f32 v18, v18, v19
	s_waitcnt lgkmcnt(0)
	v_mul_f32_e32 v19, v2, v142
	v_mul_f32_e32 v20, v3, v143
	v_cvt_pk_bf16_f32 v19, v19, v20
	v_add_u32_e32 v20, 8, v24
	v_ashrrev_i32_e32 v21, 31, v20
	v_mul_lo_u32 v22, s56, v21
	v_mul_lo_u32 v23, s57, v20
	v_mad_u64_u32 v[20:21], s[6:7], s56, v20, 0
	v_add3_u32 v21, v21, v22, v23
	v_lshl_add_u64 v[20:21], v[20:21], 1, s[60:61]
	v_lshl_add_u64 v[20:21], v[20:21], 0, s[4:5]
	v_lshl_add_u64 v[20:21], v[20:21], 0, v[8:9]
	global_store_dwordx4 v[20:21], v[16:19], off
	s_waitcnt lgkmcnt(0)
	s_nop 0
	v_mul_f32_e32 v16, v4, v144
	v_mul_f32_e32 v17, v5, v145
	v_cvt_pk_bf16_f32 v16, v16, v17
	s_waitcnt lgkmcnt(0)
	v_mul_f32_e32 v17, v6, v146
	v_mul_f32_e32 v18, v7, v147
	v_cvt_pk_bf16_f32 v17, v17, v18
	s_waitcnt lgkmcnt(0)
	v_mul_f32_e32 v18, v0, v148
	v_mul_f32_e32 v19, v1, v149
	v_cvt_pk_bf16_f32 v18, v18, v19
	s_waitcnt lgkmcnt(0)
; __device__ __forceinline__ unsigned cvt_pk_bf16(float lo, float hi) { unsigned r; asm volatile("v_cvt_pk_bf16_f32 %0, %1, %2" : "=v"(r) : "v"(lo), "v"(hi)); return r; }
; #define LAS __attribute__((address_space(3)))
; #define LDS_WAIT() asm volatile("s_waitcnt lgkmcnt(0)" ::: "memory")
; __device__ __forceinline__ void conv_store(const ConvItem& ci, LAS float* scr, int lane, const float (&v)[64]) {
;     ...
;     for (int j = 0; j < 8; ++j) { const int n = (lane >> 3) + 8 * j; const LAS float* s = scr + (8 * c) * 65 + n;
;         v4u o; o.x = cvt_pk_bf16(s[0 * 65] * s0[0], s[1 * 65] * s0[1]); o.y = cvt_pk_bf16(s[2 * 65] * s0[2], s[3 * 65] * s0[3]); o.z = cvt_pk_bf16(s[4 * 65] * s1[0], s[5 * 65] * s1[1]); o.w = cvt_pk_bf16(s[6 * 65] * s1[2], s[7 * 65] * s1[3]);
;         *(v4u*)(ci.dst + (size_t)(ci.drow0 + n) * ci.ldd + ci.k0 + 8 * c) = o; }
;     LDS_WAIT(); asm volatile("" ::: "memory");
	v_mul_f32_e32 v19, v2, v150
	v_mul_f32_e32 v20, v3, v151
	v_cvt_pk_bf16_f32 v19, v19, v20
	v_add_u32_e32 v20, 16, v24
	v_ashrrev_i32_e32 v21, 31, v20
	v_mul_lo_u32 v22, s56, v21
	v_mul_lo_u32 v23, s57, v20
	v_mad_u64_u32 v[20:21], s[6:7], s56, v20, 0
	v_add3_u32 v21, v21, v22, v23
	v_lshl_add_u64 v[20:21], v[20:21], 1, s[60:61]
	v_lshl_add_u64 v[20:21], v[20:21], 0, s[4:5]
	v_lshl_add_u64 v[20:21], v[20:21], 0, v[8:9]
	global_store_dwordx4 v[20:21], v[16:19], off
	s_waitcnt lgkmcnt(0)
	s_nop 0
	v_mul_f32_e32 v16, v4, v152
	v_mul_f32_e32 v17, v5, v153
	v_cvt_pk_bf16_f32 v16, v16, v17
	s_waitcnt lgkmcnt(0)
	v_mul_f32_e32 v17, v6, v154
	v_mul_f32_e32 v18, v7, v155
	v_cvt_pk_bf16_f32 v17, v17, v18
	s_waitcnt lgkmcnt(0)
	v_mul_f32_e32 v18, v0, v156
	v_mul_f32_e32 v19, v1, v157
	v_cvt_pk_bf16_f32 v18, v18, v19
	s_waitcnt lgkmcnt(0)
	v_mul_f32_e32 v19, v2, v158
	v_mul_f32_e32 v20, v3, v159
	v_cvt_pk_bf16_f32 v19, v19, v20
	v_add_u32_e32 v20, 24, v24
	v_ashrrev_i32_e32 v21, 31, v20
	v_mul_lo_u32 v22, s56, v21
	v_mul_lo_u32 v23, s57, v20
	v_mad_u64_u32 v[20:21], s[6:7], s56, v20, 0
	v_add3_u32 v21, v21, v22, v23
	v_lshl_add_u64 v[20:21], v[20:21], 1, s[60:61]
	v_lshl_add_u64 v[20:21], v[20:21], 0, s[4:5]
	v_lshl_add_u64 v[20:21], v[20:21], 0, v[8:9]
	global_store_dwordx4 v[20:21], v[16:19], off
	s_waitcnt lgkmcnt(0)
	s_nop 0
	v_mul_f32_e32 v16, v4, v160
	v_mul_f32_e32 v17, v5, v161
	v_cvt_pk_bf16_f32 v16, v16, v17
	s_waitcnt lgkmcnt(0)
	v_mul_f32_e32 v17, v6, v162
	v_mul_f32_e32 v18, v7, v163
	v_cvt_pk_bf16_f32 v17, v17, v18
	s_waitcnt lgkmcnt(0)
	v_mul_f32_e32 v18, v0, v164
	v_mul_f32_e32 v19, v1, v165
	v_cvt_pk_bf16_f32 v18, v18, v19
	s_waitcnt lgkmcnt(0)
	v_mul_f32_e32 v19, v2, v166
	v_mul_f32_e32 v20, v3, v167
	v_cvt_pk_bf16_f32 v19, v19, v20
	v_add_u32_e32 v20, 32, v24
	v_ashrrev_i32_e32 v21, 31, v20
	v_mul_lo_u32 v22, s56, v21
	v_mul_lo_u32 v23, s57, v20
	v_mad_u64_u32 v[20:21], s[6:7], s56, v20, 0
	v_add3_u32 v21, v21, v22, v23
	v_lshl_add_u64 v[20:21], v[20:21], 1, s[60:61]
	v_lshl_add_u64 v[20:21], v[20:21], 0, s[4:5]
	v_lshl_add_u64 v[20:21], v[20:21], 0, v[8:9]
	global_store_dwordx4 v[20:21], v[16:19], off
	s_waitcnt lgkmcnt(0)
	s_nop 0
	v_mul_f32_e32 v16, v4, v168
	v_mul_f32_e32 v17, v5, v169
	v_cvt_pk_bf16_f32 v16, v16, v17
	s_waitcnt lgkmcnt(0)
	v_mul_f32_e32 v17, v6, v170
	v_mul_f32_e32 v18, v7, v171
	v_cvt_pk_bf16_f32 v17, v17, v18
	s_waitcnt lgkmcnt(0)
	v_mul_f32_e32 v18, v0, v172
	v_mul_f32_e32 v19, v1, v173
	v_cvt_pk_bf16_f32 v18, v18, v19
	s_waitcnt lgkmcnt(0)
	v_mul_f32_e32 v19, v2, v174
	v_mul_f32_e32 v20, v3, v175
	v_cvt_pk_bf16_f32 v19, v19, v20
	v_add_u32_e32 v20, 40, v24
	v_ashrrev_i32_e32 v21, 31, v20
	v_mul_lo_u32 v22, s56, v21
	v_mul_lo_u32 v23, s57, v20
	v_mad_u64_u32 v[20:21], s[6:7], s56, v20, 0
	v_add3_u32 v21, v21, v22, v23
	v_lshl_add_u64 v[20:21], v[20:21], 1, s[60:61]
	v_lshl_add_u64 v[20:21], v[20:21], 0, s[4:5]
	v_lshl_add_u64 v[20:21], v[20:21], 0, v[8:9]
	global_store_dwordx4 v[20:21], v[16:19], off
	s_waitcnt lgkmcnt(0)
	s_nop 0
	v_mul_f32_e32 v16, v4, v176
	v_mul_f32_e32 v17, v5, v177
	v_cvt_pk_bf16_f32 v16, v16, v17
	s_waitcnt lgkmcnt(0)
	v_mul_f32_e32 v17, v6, v178
	v_mul_f32_e32 v18, v7, v179
	v_cvt_pk_bf16_f32 v17, v17, v18
	s_waitcnt lgkmcnt(0)
	v_mul_f32_e32 v18, v0, v180
	v_mul_f32_e32 v19, v1, v181
	v_cvt_pk_bf16_f32 v18, v18, v19
	s_waitcnt lgkmcnt(0)
	v_mul_f32_e32 v19, v2, v182
	v_mul_f32_e32 v20, v3, v183
	v_cvt_pk_bf16_f32 v19, v19, v20
	v_add_u32_e32 v20, 48, v24
	v_ashrrev_i32_e32 v21, 31, v20
	v_mul_lo_u32 v22, s56, v21
	v_mul_lo_u32 v23, s57, v20
	v_mad_u64_u32 v[20:21], s[6:7], s56, v20, 0
	v_add3_u32 v21, v21, v22, v23
	v_lshl_add_u64 v[20:21], v[20:21], 1, s[60:61]
	v_lshl_add_u64 v[20:21], v[20:21], 0, s[4:5]
	v_lshl_add_u64 v[20:21], v[20:21], 0, v[8:9]
	global_store_dwordx4 v[20:21], v[16:19], off
	s_waitcnt lgkmcnt(0)
	v_mul_f32_e32 v4, v4, v184
	v_mul_f32_e32 v5, v5, v185
	v_cvt_pk_bf16_f32 v4, v4, v5
	s_waitcnt lgkmcnt(0)
	v_mul_f32_e32 v5, v6, v186
	v_mul_f32_e32 v6, v7, v187
	v_cvt_pk_bf16_f32 v5, v5, v6
	s_waitcnt lgkmcnt(0)
	v_mul_f32_e32 v0, v0, v188
	v_mul_f32_e32 v1, v1, v189
	v_cvt_pk_bf16_f32 v6, v0, v1
	s_waitcnt lgkmcnt(0)
	v_mul_f32_e32 v0, v2, v190
	v_mul_f32_e32 v1, v3, v191
	v_cvt_pk_bf16_f32 v7, v0, v1
	v_add_u32_e32 v0, 56, v24
	v_ashrrev_i32_e32 v1, 31, v0
	v_mul_lo_u32 v2, s56, v1
	v_mul_lo_u32 v3, s57, v0
	v_mad_u64_u32 v[0:1], s[6:7], s56, v0, 0
	v_add3_u32 v1, v1, v2, v3
	v_lshl_add_u64 v[0:1], v[0:1], 1, s[60:61]
	v_lshl_add_u64 v[0:1], v[0:1], 0, s[4:5]
	v_lshl_add_u64 v[0:1], v[0:1], 0, v[8:9]
	global_store_dwordx4 v[0:1], v[4:7], off
	s_waitcnt lgkmcnt(0)
	s_cbranch_scc0 .Lmy_p0_second
